# router first pass: next iteration's 8 x-row pieces requested one iteration ahead into a second register set (copied into the working set at the iteration start)
# baseline (speedup 1.0000x reference)
.LBB0_1210:
	s_and_saveexec_b64 s[0:1], s[42:43]
	ds_write_b32 v63, v115
	s_or_b64 exec, exec, s[0:1]
	v_ashrrev_i32_e32 v67, 31, v66
	v_lshlrev_b64 v[76:77], 11, v[66:67]
	v_mov_b32_e32 v110, 0
	v_lshl_add_u64 v[78:79], v[70:71], 0, v[76:77]
	s_mov_b64 s[0:1], 0
	v_mov_b32_e32 v67, v108
	v_mov_b32_e32 v14, 0
	v_mov_b32_e32 v15, v110
	v_mov_b32_e32 v16, v110
	v_mov_b32_e32 v17, v110
	v_mov_b32_e32 v6, 0
	v_mov_b32_e32 v7, v110
	v_mov_b32_e32 v8, v110
	v_mov_b32_e32 v9, v110
	v_mov_b32_e32 v2, 0
	v_mov_b32_e32 v3, v110
	v_mov_b32_e32 v4, v110
	v_mov_b32_e32 v5, v110
	s_waitcnt lgkmcnt(0)
	s_barrier
	s_mov_b64 s[22:23], 0x29151000
	v_lshl_add_u64 v[120:121], v[78:79], 0, s[22:23]
	global_load_dwordx4 v[156:159], v[120:121], off offset:1280
	global_load_dwordx4 v[160:163], v[120:121], off offset:1344
	global_load_dwordx4 v[164:167], v[120:121], off offset:1408
	global_load_dwordx4 v[168:171], v[120:121], off offset:1472
	global_load_dwordx4 v[172:175], v[120:121], off offset:1536
	global_load_dwordx4 v[176:179], v[120:121], off offset:1600
	global_load_dwordx4 v[180:183], v[120:121], off offset:1664
	global_load_dwordx4 v[184:187], v[120:121], off offset:1728
	s_branch .LBB0_1214

.LBB0_1214:
	v_lshl_add_u64 v[80:81], v[78:79], 0, s[0:1]
	s_mov_b64 s[22:23], 0x29151000
	v_lshl_add_u64 v[120:121], v[80:81], 0, s[22:23]
	s_waitcnt vmcnt(0)
	v_mov_b32_e32 v124, v156
	v_mov_b32_e32 v125, v157
	v_mov_b32_e32 v126, v158
	v_mov_b32_e32 v127, v159
	v_mov_b32_e32 v128, v160
	v_mov_b32_e32 v129, v161
	v_mov_b32_e32 v130, v162
	v_mov_b32_e32 v131, v163
	v_mov_b32_e32 v132, v164
	v_mov_b32_e32 v133, v165
	v_mov_b32_e32 v134, v166
	v_mov_b32_e32 v135, v167
	v_mov_b32_e32 v136, v168
	v_mov_b32_e32 v137, v169
	v_mov_b32_e32 v138, v170
	v_mov_b32_e32 v139, v171
	v_mov_b32_e32 v140, v172
	v_mov_b32_e32 v141, v173
	v_mov_b32_e32 v142, v174
	v_mov_b32_e32 v143, v175
	v_mov_b32_e32 v144, v176
	v_mov_b32_e32 v145, v177
	v_mov_b32_e32 v146, v178
	v_mov_b32_e32 v147, v179
	v_mov_b32_e32 v148, v180
	v_mov_b32_e32 v149, v181
	v_mov_b32_e32 v150, v182
	v_mov_b32_e32 v151, v183
	v_mov_b32_e32 v152, v184
	v_mov_b32_e32 v153, v185
	v_mov_b32_e32 v154, v186
	v_mov_b32_e32 v155, v187
	s_cmpk_eq_i32 s0, 0x600
	s_cbranch_scc1 .Lr5_nopf
	global_load_dwordx4 v[156:159], v[120:121], off offset:1792
	global_load_dwordx4 v[160:163], v[120:121], off offset:1856
	global_load_dwordx4 v[164:167], v[120:121], off offset:1920
	global_load_dwordx4 v[168:171], v[120:121], off offset:1984
	global_load_dwordx4 v[172:175], v[120:121], off offset:2048
	global_load_dwordx4 v[176:179], v[120:121], off offset:2112
	global_load_dwordx4 v[180:183], v[120:121], off offset:2176
	global_load_dwordx4 v[184:187], v[120:121], off offset:2240
.Lr5_nopf:
	s_mov_b32 s22, 0x29151000
	v_add_co_u32_e32 v10, vcc, s22, v80
	v_subrev_u32_e32 v18, 28, v67
	s_nop 0
	v_addc_co_u32_e32 v11, vcc, 0, v81, vcc
	v_xor_b32_e32 v18, v18, v1
	v_lshlrev_b32_e32 v18, 4, v18
	s_add_i32 s24, 0, 0x12000
	v_add_u32_e32 v26, 0, v18
	v_add_u32_e32 v27, s24, v18
	v_lshlrev_b32_e32 v111, 1, v82
	v_add_u32_e32 v28, v27, v111
	v_add_u32_e32 v29, v26, v111
	ds_read_b128 v[18:21], v28
	ds_read_b128 v[22:25], v29
	s_waitcnt lgkmcnt(0)
	v_mfma_f32_16x16x32_bf16 v[6:9], v[124:127], v[22:25], v[6:9]
	v_mfma_f32_16x16x32_bf16 v[6:9], v[124:127], v[18:21], v[6:9]
	ds_read_b128 v[18:21], v28 offset:32768
	ds_read_b128 v[22:25], v29 offset:32768
	s_waitcnt lgkmcnt(0)
	v_mfma_f32_16x16x32_bf16 v[2:5], v[124:127], v[22:25], v[2:5]
	v_mov_b32_e32 v22, 0
	v_mov_b32_e32 v23, 0
	v_mov_b32_e32 v24, 0
	v_mfma_f32_16x16x32_bf16 v[18:21], v[124:127], v[18:21], v[2:5]
	v_mov_b32_e32 v25, 0
	s_nop 2
	v_mov_b32_e32 v2, 0
	v_mov_b32_e32 v3, 0
	v_mov_b32_e32 v4, 0
	v_mov_b32_e32 v5, 0
	s_and_saveexec_b64 s[22:23], s[44:45]
	s_cbranch_execz .LBB0_1216
	v_add_u32_e32 v2, v27, v109
	v_add_u32_e32 v3, v26, v109
	ds_read_b128 v[22:25], v3
	ds_read_b128 v[2:5], v2
.LBB0_1216:
	s_or_b64 exec, exec, s[22:23]
	s_waitcnt lgkmcnt(1)
	v_mfma_f32_16x16x32_bf16 v[14:17], v[124:127], v[22:25], v[14:17]
	v_subrev_u32_e32 v22, 24, v67
	v_xor_b32_e32 v22, v22, v1
	v_lshlrev_b32_e32 v22, 4, v22
	s_waitcnt lgkmcnt(0)
	v_mfma_f32_16x16x32_bf16 v[2:5], v[124:127], v[2:5], v[14:17]
	v_add_u32_e32 v38, 0, v22
	v_add_u32_e32 v39, s24, v22
	v_add_u32_e32 v30, v39, v111
	v_add_co_u32_e32 v14, vcc, 0x29151000, v80
	v_add_u32_e32 v31, v38, v111
	s_nop 0
	v_addc_co_u32_e32 v15, vcc, 0, v81, vcc
	ds_read_b128 v[22:25], v30
	ds_read_b128 v[26:29], v31
	v_mov_b32_e32 v32, 0
	v_mov_b32_e32 v33, 0
	v_mov_b32_e32 v34, 0
	v_mov_b32_e32 v35, 0
	v_mov_b32_e32 v36, 0
	v_mov_b32_e32 v37, 0
	s_waitcnt lgkmcnt(0)
	v_mfma_f32_16x16x32_bf16 v[6:9], v[128:131], v[26:29], v[6:9]
	v_mfma_f32_16x16x32_bf16 v[22:25], v[128:131], v[22:25], v[6:9]
	s_nop 6
	ds_read_b128 v[6:9], v30 offset:32768
	ds_read_b128 v[26:29], v31 offset:32768
	v_mov_b32_e32 v30, 0
	v_mov_b32_e32 v31, 0
	s_waitcnt lgkmcnt(0)
	v_mfma_f32_16x16x32_bf16 v[18:21], v[128:131], v[26:29], v[18:21]
	v_mfma_f32_16x16x32_bf16 v[26:29], v[128:131], v[6:9], v[18:21]
	v_mov_b32_e32 v6, 0
	s_and_saveexec_b64 s[22:23], s[44:45]
	s_cbranch_execz .LBB0_1218
	v_add_u32_e32 v8, v38, v109
	v_add_u32_e32 v7, v39, v109
	ds_read_b128 v[34:37], v8
	ds_read_b128 v[30:33], v7
.LBB0_1218:
	s_or_b64 exec, exec, s[22:23]
	v_add_co_u32_e32 v8, vcc, 0x29151000, v80
	v_subrev_u32_e32 v7, 20, v67
	s_nop 0
	v_addc_co_u32_e32 v9, vcc, 0, v81, vcc
	s_waitcnt lgkmcnt(1)
	v_mfma_f32_16x16x32_bf16 v[2:5], v[128:131], v[34:37], v[2:5]
	v_xor_b32_e32 v7, v7, v1
	v_lshlrev_b32_e32 v7, 4, v7
	v_add_u32_e32 v34, 0, v7
	v_add_u32_e32 v8, v34, v111
	s_waitcnt lgkmcnt(0)
	v_mfma_f32_16x16x32_bf16 v[2:5], v[128:131], v[30:33], v[2:5]
	ds_read_b128 v[30:33], v8
	ds_read_b128 v[36:39], v8 offset:32768
	v_add_u32_e32 v35, s24, v7
	v_add_u32_e32 v7, v35, v111
	v_mov_b32_e32 v8, 0
	v_mov_b32_e32 v9, 0
	s_waitcnt lgkmcnt(1)
	v_mfma_f32_16x16x32_bf16 v[22:25], v[132:135], v[30:33], v[22:25]
	s_waitcnt lgkmcnt(0)
	v_mfma_f32_16x16x32_bf16 v[26:29], v[132:135], v[36:39], v[26:29]
	ds_read_b128 v[30:33], v7
	ds_read_b128 v[36:39], v7 offset:32768
	v_mov_b32_e32 v7, 0
	s_waitcnt lgkmcnt(1)
	v_mfma_f32_16x16x32_bf16 v[30:33], v[132:135], v[30:33], v[22:25]
	s_nop 2
	v_mov_b32_e32 v22, 0
	s_waitcnt lgkmcnt(0)
	v_mfma_f32_16x16x32_bf16 v[26:29], v[132:135], v[36:39], v[26:29]
	v_mov_b32_e32 v23, 0
	v_mov_b32_e32 v24, 0
	v_mov_b32_e32 v25, 0
	s_and_saveexec_b64 s[22:23], s[44:45]
	s_cbranch_execz .LBB0_1220
	v_add_u32_e32 v6, v35, v109
	v_add_u32_e32 v7, v34, v109
	ds_read_b128 v[22:25], v7
	ds_read_b128 v[6:9], v6
.LBB0_1220:
	s_or_b64 exec, exec, s[22:23]
	s_waitcnt lgkmcnt(1)
	v_mfma_f32_16x16x32_bf16 v[2:5], v[132:135], v[22:25], v[2:5]
	v_mov_b32_e32 v42, 0
	v_mov_b32_e32 v43, 0
	v_mov_b32_e32 v44, 0
	s_waitcnt lgkmcnt(0)
	v_mfma_f32_16x16x32_bf16 v[2:5], v[132:135], v[6:9], v[2:5]
	v_add_co_u32_e32 v6, vcc, 0x29151000, v80
	v_mov_b32_e32 v45, 0
	s_nop 0
	v_addc_co_u32_e32 v7, vcc, 0, v81, vcc
	v_add_u32_e32 v6, -16, v67
	v_xor_b32_e32 v6, v6, v1
	v_lshlrev_b32_e32 v6, 4, v6
	v_add_u32_e32 v7, 0, v6
	v_add_u32_e32 v8, s24, v6
	v_add_u32_e32 v6, v8, v111
	v_add_u32_e32 v9, v7, v111
	ds_read_b128 v[34:37], v6
	ds_read_b128 v[38:41], v9
	s_waitcnt lgkmcnt(0)
	v_mfma_f32_16x16x32_bf16 v[30:33], v[136:139], v[38:41], v[30:33]
	v_mfma_f32_16x16x32_bf16 v[30:33], v[136:139], v[34:37], v[30:33]
	ds_read_b128 v[34:37], v6 offset:32768
	ds_read_b128 v[38:41], v9 offset:32768
	v_mov_b32_e32 v6, 0
	s_waitcnt lgkmcnt(0)
	v_mfma_f32_16x16x32_bf16 v[26:29], v[136:139], v[38:41], v[26:29]
	v_mov_b32_e32 v38, 0
	v_mov_b32_e32 v39, 0
	v_mov_b32_e32 v40, 0
	v_mfma_f32_16x16x32_bf16 v[34:37], v[136:139], v[34:37], v[26:29]
	v_mov_b32_e32 v41, 0
	s_and_saveexec_b64 s[22:23], s[44:45]
	s_cbranch_execz .LBB0_1222
	v_add_u32_e32 v7, v7, v109
	v_add_u32_e32 v8, v8, v109
	ds_read_b128 v[42:45], v7
	ds_read_b128 v[38:41], v8
.LBB0_1222:
	s_or_b64 exec, exec, s[22:23]
	v_add_co_u32_e32 v8, vcc, 0x29151000, v80
	v_add_u32_e32 v7, -12, v67
	s_nop 0
	v_addc_co_u32_e32 v9, vcc, 0, v81, vcc
	s_waitcnt lgkmcnt(1)
	v_mfma_f32_16x16x32_bf16 v[2:5], v[136:139], v[42:45], v[2:5]
	v_xor_b32_e32 v7, v7, v1
	v_lshlrev_b32_e32 v7, 4, v7
	v_add_u32_e32 v42, 0, v7
	v_add_u32_e32 v8, v42, v111
	s_waitcnt lgkmcnt(0)
	v_mfma_f32_16x16x32_bf16 v[2:5], v[136:139], v[38:41], v[2:5]
	ds_read_b128 v[38:41], v8
	ds_read_b128 v[44:47], v8 offset:32768
	v_add_u32_e32 v43, s24, v7
	v_add_u32_e32 v7, v43, v111
	v_mov_b32_e32 v8, 0
	v_mov_b32_e32 v9, 0
	s_waitcnt lgkmcnt(1)
	v_mfma_f32_16x16x32_bf16 v[30:33], v[140:143], v[38:41], v[30:33]
	s_waitcnt lgkmcnt(0)
	v_mfma_f32_16x16x32_bf16 v[34:37], v[140:143], v[44:47], v[34:37]
	ds_read_b128 v[38:41], v7
	ds_read_b128 v[44:47], v7 offset:32768
	v_mov_b32_e32 v7, 0
	s_waitcnt lgkmcnt(1)
	v_mfma_f32_16x16x32_bf16 v[38:41], v[140:143], v[38:41], v[30:33]
	s_nop 2
	v_mov_b32_e32 v30, 0
	s_waitcnt lgkmcnt(0)
	v_mfma_f32_16x16x32_bf16 v[34:37], v[140:143], v[44:47], v[34:37]
	v_mov_b32_e32 v31, 0
	v_mov_b32_e32 v32, 0
	v_mov_b32_e32 v33, 0
	s_and_saveexec_b64 s[22:23], s[44:45]
	s_cbranch_execz .LBB0_1224
	v_add_u32_e32 v6, v43, v109
	v_add_u32_e32 v7, v42, v109
	ds_read_b128 v[30:33], v7
	ds_read_b128 v[6:9], v6
.LBB0_1224:
	s_or_b64 exec, exec, s[22:23]
	s_waitcnt lgkmcnt(1)
	v_mfma_f32_16x16x32_bf16 v[2:5], v[140:143], v[30:33], v[2:5]
	v_mov_b32_e32 v50, 0
	v_mov_b32_e32 v51, 0
	v_mov_b32_e32 v52, 0
	s_waitcnt lgkmcnt(0)
	v_mfma_f32_16x16x32_bf16 v[4:7], v[140:143], v[6:9], v[2:5]
	v_mov_b32_e32 v53, 0
	s_nop 1
	v_add_co_u32_e32 v2, vcc, 0x29151000, v80
	s_nop 1
	v_addc_co_u32_e32 v3, vcc, 0, v81, vcc
	v_add_u32_e32 v2, -8, v67
	v_xor_b32_e32 v2, v2, v1
	v_lshlrev_b32_e32 v2, 4, v2
	v_add_u32_e32 v3, 0, v2
	v_add_u32_e32 v8, s24, v2
	v_add_u32_e32 v2, v8, v111
	v_add_u32_e32 v9, v3, v111
	ds_read_b128 v[42:45], v2
	ds_read_b128 v[46:49], v9
	s_waitcnt lgkmcnt(0)
	v_mfma_f32_16x16x32_bf16 v[38:41], v[144:147], v[46:49], v[38:41]
	v_mfma_f32_16x16x32_bf16 v[38:41], v[144:147], v[42:45], v[38:41]
	ds_read_b128 v[42:45], v2 offset:32768
	ds_read_b128 v[46:49], v9 offset:32768
	v_mov_b32_e32 v2, 0
	s_waitcnt lgkmcnt(0)
	v_mfma_f32_16x16x32_bf16 v[34:37], v[144:147], v[46:49], v[34:37]
	v_mov_b32_e32 v46, 0
	v_mov_b32_e32 v47, 0
	v_mov_b32_e32 v48, 0
	v_mfma_f32_16x16x32_bf16 v[42:45], v[144:147], v[42:45], v[34:37]
	v_mov_b32_e32 v49, 0
	s_and_saveexec_b64 s[22:23], s[44:45]
	s_cbranch_execz .LBB0_1226
	v_add_u32_e32 v3, v3, v109
	v_add_u32_e32 v8, v8, v109
	ds_read_b128 v[50:53], v3
	ds_read_b128 v[46:49], v8
.LBB0_1226:
	s_or_b64 exec, exec, s[22:23]
	v_add_co_u32_e32 v8, vcc, 0x29151000, v80
	v_add_u32_e32 v3, -4, v67
	s_nop 0
	v_addc_co_u32_e32 v9, vcc, 0, v81, vcc
	s_waitcnt lgkmcnt(1)
	v_mfma_f32_16x16x32_bf16 v[4:7], v[144:147], v[50:53], v[4:7]
	v_xor_b32_e32 v3, v3, v1
	v_lshlrev_b32_e32 v3, 4, v3
	v_add_u32_e32 v112, 0, v3
	v_add_u32_e32 v8, v112, v111
	s_waitcnt lgkmcnt(0)
	v_mfma_f32_16x16x32_bf16 v[50:53], v[144:147], v[46:49], v[4:7]
	s_nop 2
	ds_read_b128 v[4:7], v8
	ds_read_b128 v[46:49], v8 offset:32768
	s_waitcnt lgkmcnt(1)
	v_mfma_f32_16x16x32_bf16 v[4:7], v[148:151], v[4:7], v[38:41]
	s_nop 2
	v_add_u32_e32 v38, s24, v3
	v_add_u32_e32 v3, v38, v111
	s_waitcnt lgkmcnt(0)
	v_mfma_f32_16x16x32_bf16 v[40:43], v[148:151], v[46:49], v[42:45]
	s_nop 2
	ds_read_b128 v[44:47], v3
	ds_read_b128 v[116:119], v3 offset:32768
	v_mov_b32_e32 v3, 0
	s_waitcnt lgkmcnt(1)
	v_mfma_f32_16x16x32_bf16 v[46:49], v[148:151], v[44:47], v[4:7]
	v_mov_b32_e32 v44, 0
	v_mov_b32_e32 v45, 0
	s_nop 0
	v_mov_b32_e32 v4, 0
	s_waitcnt lgkmcnt(0)
	v_mfma_f32_16x16x32_bf16 v[6:9], v[148:151], v[116:119], v[40:43]
	v_mov_b32_e32 v5, 0
	s_nop 1
	v_mov_b32_e32 v42, 0
	v_mov_b32_e32 v43, 0
	s_and_saveexec_b64 s[22:23], s[44:45]
	s_cbranch_execz .LBB0_1228
	v_add_u32_e32 v2, v38, v109
	v_add_u32_e32 v3, v112, v109
	ds_read_b128 v[42:45], v3
	ds_read_b128 v[2:5], v2
.LBB0_1228:
	s_or_b64 exec, exec, s[22:23]
	v_add_co_u32_e32 v38, vcc, 0x29151000, v80
	s_waitcnt lgkmcnt(1)
	v_mfma_f32_16x16x32_bf16 v[42:45], v[148:151], v[42:45], v[50:53]
	v_addc_co_u32_e32 v39, vcc, 0, v81, vcc
	s_nop 0
	v_xor_b32_e32 v50, v67, v1
	v_lshlrev_b32_e32 v81, 4, v50
	v_add_u32_e32 v80, 0, v81
	v_add_u32_e32 v50, v80, v111
	s_waitcnt lgkmcnt(0)
	v_mfma_f32_16x16x32_bf16 v[42:45], v[148:151], v[2:5], v[42:45]
	ds_read_b128 v[2:5], v50
	ds_read_b128 v[50:53], v50 offset:32768
	v_add_u32_e32 v81, s24, v81
	s_waitcnt lgkmcnt(1)
	v_mfma_f32_16x16x32_bf16 v[2:5], v[152:155], v[2:5], v[46:49]
	s_nop 2
	v_add_u32_e32 v47, v81, v111
	ds_read_b128 v[116:119], v47 offset:32768
	v_mov_b32_e32 v46, 0
	s_waitcnt lgkmcnt(1)
	v_mfma_f32_16x16x32_bf16 v[50:53], v[152:155], v[50:53], v[6:9]
	v_mov_b32_e32 v48, 0
	v_mov_b32_e32 v49, 0
	s_nop 0
	ds_read_b128 v[6:9], v47
	s_waitcnt lgkmcnt(0)
	v_mfma_f32_16x16x32_bf16 v[6:9], v[152:155], v[6:9], v[2:5]
	v_mov_b32_e32 v47, 0
	v_mfma_f32_16x16x32_bf16 v[2:5], v[152:155], v[116:119], v[50:53]
	s_nop 2
	v_mov_b32_e32 v50, 0
	v_mov_b32_e32 v51, 0
	v_mov_b32_e32 v52, 0
	v_mov_b32_e32 v53, 0
	s_and_saveexec_b64 s[22:23], s[44:45]
	s_cbranch_execz .LBB0_1213
	v_add_u32_e32 v46, v81, v109
	v_add_u32_e32 v47, v80, v109
	ds_read_b128 v[50:53], v47
	ds_read_b128 v[46:49], v46
	s_branch .LBB0_1213
